# v33 + SB unit loop: grid size kept in an SGPR instead of a kernarg s_load (and its wait) at every unit boundary
# speedup vs baseline: 1.0020x; 1.0020x over previous
; #define GAS __attribute__((address_space(1)))
; #define GAS __attribute__((address_space(1)))
; __device__ __forceinline__ float xor32(float x) { auto rr = __builtin_amdgcn_permlane32_swap(__float_as_uint(x), __float_as_uint(x), false, false); return __uint_as_float(((unsigned)(threadIdx.x & 32)) ? rr[0] : rr[1]); }
; __device__ __forceinline__ unsigned cvtpk(float lo, float hi) { f32x2 v = {lo, hi}; bf16x2_t b = __builtin_convertvector(v, bf16x2_t); return __builtin_bit_cast(unsigned, b); }
; __device__ __forceinline__ void store_o(bf16_t* orow, const f32x16& o0, const f32x16& o1, int hi, float sc, float* oss) {
;     float sq = 0.f;
; #pragma unroll
;     for (int r = 0; r < 16; ++r) sq += o0[r] * o0[r] + o1[r] * o1[r];
;     sq = (sq + xor32(sq)) * (sc * sc);
;     if (hi == 0) *(GAS float*)oss = sq;
; #pragma unroll
;     for (int half = 0; half < 2; ++half) {
;         const f32x16& o = half ? o1 : o0;
; #pragma unroll
;         for (int k = 0; k < 4; k += 2) {
;             unsigned ax = cvtpk(o[4 * k] * sc, o[4 * k + 1] * sc), ay = cvtpk(o[4 * k + 2] * sc, o[4 * k + 3] * sc);
;             unsigned bx = cvtpk(o[4 * k + 4] * sc, o[4 * k + 5] * sc), by = cvtpk(o[4 * k + 6] * sc, o[4 * k + 7] * sc);
;             { auto r = __builtin_amdgcn_permlane32_swap(ax, bx, false, false); ax = r[0]; bx = r[1]; }
;             { auto r = __builtin_amdgcn_permlane32_swap(ay, by, false, false); ay = r[0]; by = r[1]; }
;             *(GAS u32x4*)(orow + 32 * half + 8 * k + 8 * hi) = (u32x4){ax, ay, bx, by};
;         }
;     }
; }
; __device__ __forceinline__ void phase_attn(Frame& F) {
;     ...
;     for (int u = vcu; u < 1024; u += F.G) { const int bh = u >> 4; att::sb_unit(F.lds, F.tid, QKV, OA, OSS, bh >> 3, bh & 7, u & 15); }
.LBB0_873:
	v_readlane_b32 s2, v254, 1
	v_readlane_b32 s3, v254, 2
	s_andn2_b64 vcc, exec, s[2:3]
	s_cbranch_vccnz .LBB0_893
	s_add_u32 s2, s74, 0x12e00000
	v_writelane_b32 v255, s2, 40
	s_addc_u32 s2, s75, 0
	v_writelane_b32 v255, s2, 41
	s_load_dword s101, s[0:1], 0x110
	s_mov_b32 s78, s79
	s_mov_b64 s[28:29], 0x400
	s_mov_b64 s[30:31], 0x800
	s_branch .LBB0_876
.LBB0_875:
	s_or_b64 exec, exec, s[8:9]
	v_readlane_b32 s2, v255, 36
	v_lshlrev_b64 v[34:35], 11, v[34:35]
	v_readlane_b32 s3, v255, 37
	v_lshlrev_b32_e32 v0, 1, v114
	v_cvt_pk_bf16_f32 v18, v18, v19
	v_lshl_add_u64 v[34:35], s[2:3], 0, v[34:35]
	v_readlane_b32 s2, v255, 43
	s_lshl_b32 s88, s2, 1
	v_lshl_add_u64 v[34:35], v[34:35], 0, s[88:89]
	v_cvt_pk_bf16_f32 v19, v20, v21
	v_cvt_pk_bf16_f32 v20, v22, v23
	v_cvt_pk_bf16_f32 v21, v24, v25
	v_cvt_pk_bf16_f32 v2, v2, v3
	v_cvt_pk_bf16_f32 v3, v4, v5
	v_cvt_pk_bf16_f32 v4, v6, v7
	v_cvt_pk_bf16_f32 v5, v8, v9
	v_lshl_add_u64 v[34:35], v[34:35], 0, v[0:1]
	v_permlane32_swap_b32_e32 v18, v20
	v_permlane32_swap_b32_e32 v19, v21
	v_permlane32_swap_b32_e32 v2, v4
	v_permlane32_swap_b32_e32 v3, v5
	global_store_dwordx4 v[34:35], v[18:21], off
	global_store_dwordx4 v[34:35], v[2:5], off offset:64
	s_nop 0
	v_cvt_pk_bf16_f32 v18, v26, v27
	v_cvt_pk_bf16_f32 v19, v28, v29
	v_cvt_pk_bf16_f32 v20, v30, v31
	v_cvt_pk_bf16_f32 v21, v32, v33
	v_cvt_pk_bf16_f32 v2, v10, v11
	v_cvt_pk_bf16_f32 v3, v12, v13
	v_cvt_pk_bf16_f32 v4, v14, v15
	v_cvt_pk_bf16_f32 v5, v16, v17
	v_permlane32_swap_b32_e32 v18, v20
	v_permlane32_swap_b32_e32 v19, v21
	v_permlane32_swap_b32_e32 v2, v4
	v_permlane32_swap_b32_e32 v3, v5
	global_store_dwordx4 v[34:35], v[18:21], off offset:32
	global_store_dwordx4 v[34:35], v[2:5], off offset:96
	s_waitcnt lgkmcnt(0)
	s_barrier
	s_mov_b32 s76, s101
	s_add_i32 s79, s79, s76
	s_add_i32 s78, s78, s76
	s_cmpk_lt_i32 s79, 0x400
	s_cbranch_scc0 .LBB0_892
